# attention: rigorous diagonal+Cauchy-Schwarz screening of frames fq+-2 (exact same-position q.k via fma_mix, CS bound for the rest) so they are not streamed/visited; first barrier vmcnt(16)
# speedup vs baseline: 1.0526x; 1.0223x over previous
.LBB2_2:
	s_or_b64 exec, exec, s[12:13]
	s_lshr_b32 s2, s2, 3
	s_mul_hi_u32 s3, s2, 0x15555556
	s_mul_i32 s3, s3, 12
	s_lshr_b32 s19, s16, 6
	s_sub_i32 s20, s2, s3
	s_lshl_b32 s18, s19, 5
	s_mul_i32 s3, s6, 0xc00
	s_lshl_b32 s4, s20, 8
	v_and_b32_e32 v162, 31, v0
	s_mul_hi_u32 s2, s6, 0xc00
	s_add_u32 s12, s3, s4
	v_or_b32_e32 v2, s18, v162
	s_addc_u32 s13, s2, 0
	v_mov_b32_e32 v3, 0
	v_lshl_add_u64 v[4:5], s[12:13], 0, v[2:3]
	v_bfe_u32 v1, v0, 5, 1
	v_lshlrev_b64 v[4:5], 7, v[4:5]
	s_waitcnt lgkmcnt(0)
	v_lshl_add_u64 v[4:5], s[8:9], 0, v[4:5]
	v_lshlrev_b32_e32 v148, 4, v1
	v_mov_b32_e32 v149, v3
	v_lshl_add_u64 v[4:5], v[4:5], 0, v[148:149]
	global_load_dwordx4 v[96:99], v[4:5], off nt
	global_load_dwordx4 v[100:103], v[4:5], off offset:32 nt
	global_load_dwordx4 v[104:107], v[4:5], off offset:64 nt
	global_load_dwordx4 v[108:111], v[4:5], off offset:96 nt
	s_sub_u32 s44, s10, s8
	s_subb_u32 s45, s11, s9
	s_add_i32 s46, s20, 2
	s_cmp_gt_u32 s46, 11
	s_cselect_b32 s47, 12, 0
	s_sub_i32 s46, s46, s47
	s_mov_b32 s42, s46
	s_sub_i32 s46, s46, s20
	s_lshl_b32 s46, s46, 15
	s_ashr_i32 s47, s46, 31
	s_add_u32 s46, s46, s44
	s_addc_u32 s47, s47, s45
	v_lshl_add_u64 v[202:203], v[4:5], 0, s[46:47]
	s_add_i32 s46, s20, 10
	s_cmp_gt_u32 s46, 11
	s_cselect_b32 s47, 12, 0
	s_sub_i32 s46, s46, s47
	s_mov_b32 s43, s46
	s_sub_i32 s46, s46, s20
	s_lshl_b32 s46, s46, 15
	s_ashr_i32 s47, s46, 31
	s_add_u32 s46, s46, s44
	s_addc_u32 s47, s47, s45
	v_lshl_add_u64 v[204:205], v[4:5], 0, s[46:47]
	v_bfe_u32 v6, v0, 3, 3
	s_mul_i32 s2, s6, 0x60000
	v_lshl_or_b32 v6, s19, 3, v6
	s_mov_b32 s7, 0
	s_mul_hi_u32 s3, s6, 0x60000
	v_mov_b32_e32 v9, v3
	v_mov_b32_e32 v11, v3
	v_mov_b32_e32 v7, v3
	v_lshrrev_b32_e32 v3, 1, v6
	s_add_u32 s2, s10, s2
	v_xor_b32_e32 v3, v3, v0
	s_addc_u32 s3, s11, s3
	s_lshl_b64 s[4:5], s[6:7], 6
	s_movk_i32 s8, 0x1800
	v_mov_b64_e32 v[4:5], s[14:15]
	v_lshlrev_b32_e32 v8, 7, v6
	v_lshlrev_b32_e32 v3, 4, v3
	v_lshl_add_u64 v[6:7], s[4:5], 0, v[6:7]
	v_and_b32_e32 v10, 0x70, v3
	v_lshl_add_u64 v[8:9], s[2:3], 0, v[8:9]
	v_mad_u64_u32 v[4:5], s[2:3], v6, s8, v[4:5]
	s_lshl_b32 s9, s20, 2
	s_lshl_b32 s6, s20, 15
	v_lshl_add_u64 v[150:151], v[8:9], 0, v[10:11]
	v_mad_u32_u24 v5, v7, s8, v5
	s_or_b32 s4, s9, 1
	v_lshl_add_u64 v[6:7], v[150:151], 0, s[6:7]
	s_lshl_b32 s6, s20, 9
	v_lshl_add_u64 v[152:153], v[4:5], 0, v[10:11]
	v_lshl_add_u64 v[4:5], v[152:153], 0, s[6:7]
	s_lshl_b32 s6, s4, 13
	s_or_b32 s5, s9, 2
	v_lshl_add_u64 v[8:9], v[150:151], 0, s[6:7]
	s_lshl_b32 s6, s4, 7
	v_lshl_add_u64 v[10:11], v[152:153], 0, s[6:7]
	s_lshl_b32 s6, s5, 13
	s_or_b32 s17, s9, 3
	v_lshl_add_u64 v[12:13], v[150:151], 0, s[6:7]
	s_lshl_b32 s6, s5, 7
	s_lshl_b32 s21, s19, 10
	v_lshl_add_u64 v[14:15], v[152:153], 0, s[6:7]
	s_lshl_b32 s6, s17, 13
	s_add_i32 s22, s21, 0x2000
	s_add_i32 s10, s21, 0x4000
	s_add_i32 s11, s21, 0x6000
	s_add_i32 s14, s21, 0x8000
	s_add_i32 s15, s21, 0xa000
	s_add_i32 s23, s21, 0xc000
	s_add_i32 s24, s21, 0xe000
	v_lshl_add_u64 v[16:17], v[150:151], 0, s[6:7]
	s_lshl_b32 s6, s17, 7
	s_cmp_gt_u32 s20, 10
	s_cselect_b32 s2, -11, 1
	s_add_i32 s2, s2, s20
	v_lshl_add_u64 v[18:19], v[152:153], 0, s[6:7]
	s_lshl_b32 s6, s2, 2
	s_lshl_b64 s[4:5], s[6:7], 13
	s_waitcnt vmcnt(0)
	v_lshl_add_u64 v[20:21], v[150:151], 0, s[4:5]
	s_add_i32 s3, s21, 0x10000
	s_lshl_b32 s2, s2, 9
	s_add_i32 s9, s9, -4
	v_and_b32_e32 v149, 15, v0
	s_waitcnt vmcnt(3)
	s_waitcnt vmcnt(2)
	s_waitcnt vmcnt(1)
	s_waitcnt vmcnt(0)
	s_mov_b32 s4, m0
	s_mov_b32 m0, s21
	s_nop 0
	global_load_lds_dwordx4 v[6:7], off
	s_mov_b32 m0, s4
	s_nop 0
	s_mov_b32 s4, m0
	s_mov_b32 m0, s22
	s_nop 0
	global_load_lds_dwordx4 v[4:5], off
	s_mov_b32 m0, s4
	s_nop 0
	s_mov_b32 s4, m0
	s_mov_b32 m0, s10
	s_nop 0
	global_load_lds_dwordx4 v[8:9], off
	s_mov_b32 m0, s4
	s_nop 0
	s_mov_b32 s4, m0
	s_mov_b32 m0, s11
	s_nop 0
	global_load_lds_dwordx4 v[10:11], off
	s_mov_b32 m0, s4
	s_nop 0
	s_mov_b32 s4, m0
	s_mov_b32 m0, s14
	s_nop 0
	global_load_lds_dwordx4 v[12:13], off
	s_mov_b32 m0, s4
	s_nop 0
	s_mov_b32 s4, m0
	s_mov_b32 m0, s15
	s_nop 0
	global_load_lds_dwordx4 v[14:15], off
	s_mov_b32 m0, s4
	s_nop 0
	s_mov_b32 s4, m0
	s_mov_b32 m0, s23
	s_nop 0
	global_load_lds_dwordx4 v[16:17], off
	s_mov_b32 m0, s4
	s_nop 0
	s_mov_b32 s4, m0
	s_mov_b32 m0, s24
	s_nop 0
	global_load_lds_dwordx4 v[18:19], off
	s_mov_b32 m0, s4
	s_nop 0
	s_mov_b32 s4, m0
	s_mov_b32 m0, s3
	s_nop 0
	global_load_lds_dwordx4 v[20:21], off
	s_mov_b32 m0, s4
	s_mov_b32 s3, s7
	v_lshl_add_u64 v[4:5], v[152:153], 0, s[2:3]
	s_add_i32 s2, s21, 0x12000
	s_mov_b32 s3, m0
	s_mov_b32 m0, s2
	s_nop 0
	global_load_lds_dwordx4 v[4:5], off
	s_mov_b32 m0, s3
	s_or_b32 s2, s6, 1
	s_mov_b32 s3, s7
	s_lshl_b64 s[4:5], s[2:3], 13
	s_add_i32 s3, s21, 0x14000
	v_lshl_add_u64 v[4:5], v[150:151], 0, s[4:5]
	s_mov_b32 s4, m0
	s_mov_b32 m0, s3
	s_nop 0
	global_load_lds_dwordx4 v[4:5], off
	s_mov_b32 m0, s4
	s_lshl_b32 s2, s2, 7
	s_mov_b32 s3, s7
	v_lshl_add_u64 v[4:5], v[152:153], 0, s[2:3]
	s_add_i32 s2, s21, 0x16000
	s_mov_b32 s3, m0
	s_mov_b32 m0, s2
	s_nop 0
	global_load_lds_dwordx4 v[4:5], off
	s_mov_b32 m0, s3
	s_or_b32 s2, s6, 2
	s_mov_b32 s3, s7
	s_lshl_b64 s[4:5], s[2:3], 13
	s_add_i32 s3, s21, 0x18000
	v_lshl_add_u64 v[4:5], v[150:151], 0, s[4:5]
	s_mov_b32 s4, m0
	s_mov_b32 m0, s3
	s_nop 0
	global_load_lds_dwordx4 v[4:5], off
	s_mov_b32 m0, s4
	s_lshl_b32 s2, s2, 7
	s_mov_b32 s3, s7
	v_lshl_add_u64 v[4:5], v[152:153], 0, s[2:3]
	s_add_i32 s2, s21, 0x1a000
	s_mov_b32 s3, m0
	s_mov_b32 m0, s2
	s_nop 0
	global_load_lds_dwordx4 v[4:5], off
	s_mov_b32 m0, s3
	s_or_b32 s6, s6, 3
	s_lshl_b64 s[2:3], s[6:7], 13
	v_lshl_add_u64 v[4:5], v[150:151], 0, s[2:3]
	s_add_i32 s2, s21, 0x1c000
	s_mov_b32 s3, m0
	s_mov_b32 m0, s2
	s_nop 0
	global_load_lds_dwordx4 v[4:5], off
	s_mov_b32 m0, s3
	s_lshl_b32 s6, s6, 7
	s_add_i32 s2, s21, 0x1e000
	s_cmp_lg_u32 s20, 0
	v_lshl_add_u64 v[4:5], v[152:153], 0, s[6:7]
	s_mov_b32 s3, m0
	s_mov_b32 m0, s2
	s_nop 0
	global_load_lds_dwordx4 v[4:5], off
	s_mov_b32 m0, s3
	s_cselect_b32 s2, s9, 44
	s_ashr_i32 s3, s2, 31
	s_lshl_b64 s[4:5], s[2:3], 13
	v_lshl_add_u64 v[4:5], v[150:151], 0, s[4:5]
	s_lshl_b32 s4, s2, 6
	s_ashr_i32 s5, s4, 31
	global_load_dwordx4 v[112:115], v[4:5], off
	v_lshl_add_u64 v[4:5], s[4:5], 1, v[152:153]
	s_or_b32 s4, s2, 1
	s_ashr_i32 s5, s4, 31
	s_lshl_b64 s[6:7], s[4:5], 13
	s_lshl_b32 s4, s4, 6
	global_load_dwordx4 v[116:119], v[4:5], off
	v_lshl_add_u64 v[4:5], v[150:151], 0, s[6:7]
	s_ashr_i32 s5, s4, 31
	global_load_dwordx4 v[120:123], v[4:5], off
	v_lshl_add_u64 v[4:5], s[4:5], 1, v[152:153]
	s_or_b32 s4, s2, 2
	s_ashr_i32 s5, s4, 31
	s_lshl_b64 s[6:7], s[4:5], 13
	s_lshl_b32 s4, s4, 6
	s_or_b32 s2, s2, 3
	global_load_dwordx4 v[124:127], v[4:5], off
	v_lshl_add_u64 v[4:5], v[150:151], 0, s[6:7]
	s_ashr_i32 s5, s4, 31
	s_ashr_i32 s3, s2, 31
	global_load_dwordx4 v[128:131], v[4:5], off
	v_lshl_add_u64 v[4:5], s[4:5], 1, v[152:153]
	s_lshl_b64 s[4:5], s[2:3], 13
	s_lshl_b32 s2, s2, 6
	global_load_dwordx4 v[132:135], v[4:5], off
	v_lshl_add_u64 v[4:5], v[150:151], 0, s[4:5]
	s_ashr_i32 s3, s2, 31
	global_load_dwordx4 v[136:139], v[4:5], off
	v_lshl_add_u64 v[4:5], s[2:3], 1, v[152:153]
	global_load_dwordx4 v[140:143], v[4:5], off
	global_load_dwordx4 v[210:213], v[202:203], off
	global_load_dwordx4 v[214:217], v[202:203], off offset:32
	global_load_dwordx4 v[218:221], v[202:203], off offset:64
	global_load_dwordx4 v[222:225], v[202:203], off offset:96
	global_load_dwordx4 v[226:229], v[204:205], off
	global_load_dwordx4 v[230:233], v[204:205], off offset:32
	global_load_dwordx4 v[234:237], v[204:205], off offset:64
	global_load_dwordx4 v[238:241], v[204:205], off offset:96
	s_movk_i32 s2, 0xbf
	v_cmp_lt_u32_e32 vcc, s2, v0
	s_and_saveexec_b64 s[2:3], vcc
	s_xor_b64 s[2:3], exec, s[2:3]
	v_and_b32_e32 v149, 15, v0
	s_or_saveexec_b64 s[4:5], s[2:3]
	v_and_b32_e32 v163, 63, v0
	s_xor_b64 exec, exec, s[4:5]
	s_cbranch_execz .LBB2_6
	v_lshrrev_b32_e32 v3, 4, v0
	v_cvt_f32_ubyte0_e32 v3, v3
	v_mul_f32_e32 v3, 0x3d4ccccd, v3
	v_mov_b32_e32 v4, 0x3d4ccccd
	v_cmp_lt_u32_e32 vcc, 15, v0
	s_mov_b32 s2, 0xf800000
	s_nop 0
	v_cndmask_b32_e32 v3, v4, v3, vcc
	v_mul_f32_e32 v4, 0x3e80adfd, v3
	v_mul_f32_e32 v5, 0x4f800000, v4
	v_cmp_gt_f32_e32 vcc, s2, v4
	v_mul_f32_e32 v3, 0xbda3d70a, v3
	s_nop 0
	v_cndmask_b32_e32 v4, v4, v5, vcc
	v_sqrt_f32_e32 v5, v4
	s_nop 0
	v_add_u32_e32 v6, -1, v5
	v_fma_f32 v7, -v6, v5, v4
	v_cmp_ge_f32_e64 s[2:3], 0, v7
	v_add_u32_e32 v7, 1, v5
	s_nop 0
	v_cndmask_b32_e64 v6, v5, v6, s[2:3]
	v_fma_f32 v5, -v7, v5, v4
	v_cmp_lt_f32_e64 s[2:3], 0, v5
	s_nop 1
	v_cndmask_b32_e64 v5, v6, v7, s[2:3]
	v_mul_f32_e32 v6, 0x37800000, v5
	v_cndmask_b32_e32 v5, v5, v6, vcc
	v_mov_b32_e32 v6, 0x260
	v_cmp_class_f32_e32 vcc, v4, v6
	s_nop 1
	v_cndmask_b32_e32 v4, v5, v4, vcc
	v_div_scale_f32 v5, s[2:3], v4, v4, 1.0
	v_rcp_f32_e32 v6, v5
	s_nop 0
	v_fma_f32 v7, -v5, v6, 1.0
	v_fmac_f32_e32 v6, v7, v6
	v_div_scale_f32 v7, vcc, 1.0, v4, 1.0
	v_mul_f32_e32 v8, v7, v6
	v_fma_f32 v9, -v5, v8, v7
	v_fmac_f32_e32 v8, v9, v6
	v_mul_u32_u24_e32 v9, v149, v149
	v_cvt_f32_ubyte0_e32 v9, v9
	v_div_scale_f32 v10, s[2:3], v3, v3, v9
	v_rcp_f32_e32 v11, v10
	v_fma_f32 v5, -v5, v8, v7
	v_div_fmas_f32 v5, v5, v6, v8
	s_mov_b32 s2, 0x3fb8aa3b
	v_fma_f32 v6, -v10, v11, 1.0
	v_fmac_f32_e32 v11, v6, v11
	v_div_scale_f32 v6, vcc, v9, v3, v9
	v_mul_f32_e32 v7, v6, v11
	v_fma_f32 v8, -v10, v7, v6
	v_fmac_f32_e32 v7, v8, v11
	v_fma_f32 v6, -v10, v7, v6
	v_div_fmas_f32 v6, v6, v11, v7
	v_div_fixup_f32 v3, v6, v3, v9
	v_mul_f32_e32 v6, 0x3fb8aa3b, v3
	v_fma_f32 v7, v3, s2, -v6
	v_rndne_f32_e32 v8, v6
	v_fmamk_f32 v7, v3, 0x32a5705f, v7
	v_sub_f32_e32 v6, v6, v8
	v_add_f32_e32 v6, v6, v7
	v_exp_f32_e32 v6, v6
	v_cvt_i32_f32_e32 v7, v8
	s_mov_b32 s2, 0xc2ce8ed0
	v_div_fixup_f32 v4, v5, v4, 1.0
	v_cmp_ngt_f32_e32 vcc, s2, v3
	v_ldexp_f32 v5, v6, v7
	s_mov_b32 s2, 0x42b17218
	v_cndmask_b32_e32 v5, 0, v5, vcc
	v_mov_b32_e32 v6, 0x7f800000
	v_cmp_nlt_f32_e32 vcc, s2, v3
	s_nop 1
	v_cndmask_b32_e32 v3, v6, v5, vcc
	v_mul_f32_e32 v5, v4, v3
	v_mul_f32_e32 v4, v4, v5
	v_lshlrev_b32_e32 v5, 2, v0
	v_mul_f32_e32 v4, 0x3fb8aa3b, v4
	v_or_b32_e32 v6, 0x20000, v5
	ds_write_b32 v6, v4
	v_add_u32_e32 v4, 0x20300, v5
	ds_write_b32 v4, v3

.LBB2_14:
	s_waitcnt vmcnt(16) lgkmcnt(0)
	s_barrier
	s_cmp_lg_u32 s23, 1
	s_cbranch_scc1 .LBB2_13
.LBB2_15:
	ds_read_b128 v[34:37], v186
	ds_read_b128 v[38:41], v187
	ds_read_b128 v[42:45], v188
	ds_read_b128 v[64:67], v189
	s_waitcnt lgkmcnt(3)
	v_max_f32_e32 v33, v35, v35
	v_max_f32_e32 v34, v34, v34
	s_waitcnt lgkmcnt(2)
	v_max_f32_e32 v35, v39, v39
	v_max_f32_e32 v38, v38, v38
	v_max_f32_e32 v33, v34, v33
	v_min_f32_e32 v34, v38, v35
	v_max3_f32 v33, v33, v36, v37
	v_min3_f32 v38, v34, v40, v41
	ds_read_b128 v[34:37], v190
	ds_read_b32 v39, v191
	s_waitcnt lgkmcnt(3)
	v_max3_f32 v33, v33, v42, v43
	s_waitcnt lgkmcnt(2)
	v_min3_f32 v38, v38, v64, v65
	v_max3_f32 v33, v33, v44, v45
	s_waitcnt lgkmcnt(1)
	v_max_f32_e32 v37, v37, v37
	v_max_f32_e32 v36, v36, v36
	v_max_f32_e32 v36, v36, v37
	v_max3_f32 v34, v34, v35, v36
	v_min3_f32 v38, v38, v66, v67
	s_waitcnt lgkmcnt(0)
	v_fmac_f32_e32 v39, v33, v34
	v_sub_f32_e32 v33, v39, v38
	v_cmp_ngt_f32_e32 vcc, s26, v33
	s_and_b64 s[4:5], s[0:1], vcc
	v_cndmask_b32_e64 v33, 0, 1, s[4:5]
	v_cmp_ne_u32_e64 s[4:5], 0, v33
	v_mov_b32_e32 v34, 0x20700
	ds_read_b128 v[36:39], v34
	ds_read_b128 v[40:43], v34 offset:16
	s_waitcnt lgkmcnt(0)
	v_or3_b32 v36, v36, v37, v38
	v_or3_b32 v40, v40, v41, v42
	v_or3_b32 v36, v36, v39, v40
	v_or_b32_e32 v36, v36, v43
	s_nop 0
	v_readfirstlane_b32 s50, v36
	s_nop 3
	s_or_b32 s50, s50, 0xfffffbfb
	s_and_b32 s4, s4, s50
	s_andn2_b64 vcc, exec, s[14:15]
	s_mov_b32 s5, 1
	s_cbranch_vccnz .LBB2_22

.LBB2_38:
	s_cmp_lg_u32 s23, 0
	s_cbranch_scc1 .Lattn_diag_skip
	s_waitcnt vmcnt(0)
	s_sub_i32 s46, s20, s42
	s_abs_i32 s46, s46
	s_sub_i32 s47, s20, s43
	s_abs_i32 s47, s47
	s_lshl_b32 s46, s46, 6
	s_lshl_b32 s47, s47, 6
	s_add_i32 s46, s46, 0x20000
	s_add_i32 s47, s47, 0x20000
	v_mov_b32_e32 v64, s46
	v_mov_b32_e32 v65, s47
	ds_read_b64 v[66:67], v64
	ds_read_b64 v[68:69], v65
	s_lshl_b32 s46, s42, 4
	s_lshl_b32 s47, s43, 4
	s_add_i32 s46, s46, 0x20600
	s_add_i32 s47, s47, 0x20600
	v_mov_b32_e32 v64, s46
	v_mov_b32_e32 v65, s47
	ds_read_b128 v[70:73], v64
	ds_read_b128 v[74:77], v65
	v_fma_mix_f32 v78, v96, v210, 0 op_sel_hi:[1,1,0]
	v_fma_mix_f32 v79, v96, v226, 0 op_sel_hi:[1,1,0]
	v_fma_mix_f32 v78, v96, v210, v78 op_sel:[1,1,0] op_sel_hi:[1,1,0]
	v_fma_mix_f32 v79, v96, v226, v79 op_sel:[1,1,0] op_sel_hi:[1,1,0]
	v_fma_mix_f32 v78, v97, v211, v78 op_sel_hi:[1,1,0]
	v_fma_mix_f32 v79, v97, v227, v79 op_sel_hi:[1,1,0]
	v_fma_mix_f32 v78, v97, v211, v78 op_sel:[1,1,0] op_sel_hi:[1,1,0]
	v_fma_mix_f32 v79, v97, v227, v79 op_sel:[1,1,0] op_sel_hi:[1,1,0]
	v_fma_mix_f32 v78, v98, v212, v78 op_sel_hi:[1,1,0]
	v_fma_mix_f32 v79, v98, v228, v79 op_sel_hi:[1,1,0]
	v_fma_mix_f32 v78, v98, v212, v78 op_sel:[1,1,0] op_sel_hi:[1,1,0]
	v_fma_mix_f32 v79, v98, v228, v79 op_sel:[1,1,0] op_sel_hi:[1,1,0]
	v_fma_mix_f32 v78, v99, v213, v78 op_sel_hi:[1,1,0]
	v_fma_mix_f32 v79, v99, v229, v79 op_sel_hi:[1,1,0]
	v_fma_mix_f32 v78, v99, v213, v78 op_sel:[1,1,0] op_sel_hi:[1,1,0]
	v_fma_mix_f32 v79, v99, v229, v79 op_sel:[1,1,0] op_sel_hi:[1,1,0]
	v_fma_mix_f32 v78, v100, v214, v78 op_sel_hi:[1,1,0]
	v_fma_mix_f32 v79, v100, v230, v79 op_sel_hi:[1,1,0]
	v_fma_mix_f32 v78, v100, v214, v78 op_sel:[1,1,0] op_sel_hi:[1,1,0]
	v_fma_mix_f32 v79, v100, v230, v79 op_sel:[1,1,0] op_sel_hi:[1,1,0]
	v_fma_mix_f32 v78, v101, v215, v78 op_sel_hi:[1,1,0]
	v_fma_mix_f32 v79, v101, v231, v79 op_sel_hi:[1,1,0]
	v_fma_mix_f32 v78, v101, v215, v78 op_sel:[1,1,0] op_sel_hi:[1,1,0]
	v_fma_mix_f32 v79, v101, v231, v79 op_sel:[1,1,0] op_sel_hi:[1,1,0]
	v_fma_mix_f32 v78, v102, v216, v78 op_sel_hi:[1,1,0]
	v_fma_mix_f32 v79, v102, v232, v79 op_sel_hi:[1,1,0]
	v_fma_mix_f32 v78, v102, v216, v78 op_sel:[1,1,0] op_sel_hi:[1,1,0]
	v_fma_mix_f32 v79, v102, v232, v79 op_sel:[1,1,0] op_sel_hi:[1,1,0]
	v_fma_mix_f32 v78, v103, v217, v78 op_sel_hi:[1,1,0]
	v_fma_mix_f32 v79, v103, v233, v79 op_sel_hi:[1,1,0]
	v_fma_mix_f32 v78, v103, v217, v78 op_sel:[1,1,0] op_sel_hi:[1,1,0]
	v_fma_mix_f32 v79, v103, v233, v79 op_sel:[1,1,0] op_sel_hi:[1,1,0]
	v_fma_mix_f32 v78, v104, v218, v78 op_sel_hi:[1,1,0]
	v_fma_mix_f32 v79, v104, v234, v79 op_sel_hi:[1,1,0]
	v_fma_mix_f32 v78, v104, v218, v78 op_sel:[1,1,0] op_sel_hi:[1,1,0]
	v_fma_mix_f32 v79, v104, v234, v79 op_sel:[1,1,0] op_sel_hi:[1,1,0]
	v_fma_mix_f32 v78, v105, v219, v78 op_sel_hi:[1,1,0]
	v_fma_mix_f32 v79, v105, v235, v79 op_sel_hi:[1,1,0]
	v_fma_mix_f32 v78, v105, v219, v78 op_sel:[1,1,0] op_sel_hi:[1,1,0]
	v_fma_mix_f32 v79, v105, v235, v79 op_sel:[1,1,0] op_sel_hi:[1,1,0]
	v_fma_mix_f32 v78, v106, v220, v78 op_sel_hi:[1,1,0]
	v_fma_mix_f32 v79, v106, v236, v79 op_sel_hi:[1,1,0]
	v_fma_mix_f32 v78, v106, v220, v78 op_sel:[1,1,0] op_sel_hi:[1,1,0]
	v_fma_mix_f32 v79, v106, v236, v79 op_sel:[1,1,0] op_sel_hi:[1,1,0]
	v_fma_mix_f32 v78, v107, v221, v78 op_sel_hi:[1,1,0]
	v_fma_mix_f32 v79, v107, v237, v79 op_sel_hi:[1,1,0]
	v_fma_mix_f32 v78, v107, v221, v78 op_sel:[1,1,0] op_sel_hi:[1,1,0]
	v_fma_mix_f32 v79, v107, v237, v79 op_sel:[1,1,0] op_sel_hi:[1,1,0]
	v_fma_mix_f32 v78, v108, v222, v78 op_sel_hi:[1,1,0]
	v_fma_mix_f32 v79, v108, v238, v79 op_sel_hi:[1,1,0]
	v_fma_mix_f32 v78, v108, v222, v78 op_sel:[1,1,0] op_sel_hi:[1,1,0]
	v_fma_mix_f32 v79, v108, v238, v79 op_sel:[1,1,0] op_sel_hi:[1,1,0]
	v_fma_mix_f32 v78, v109, v223, v78 op_sel_hi:[1,1,0]
	v_fma_mix_f32 v79, v109, v239, v79 op_sel_hi:[1,1,0]
	v_fma_mix_f32 v78, v109, v223, v78 op_sel:[1,1,0] op_sel_hi:[1,1,0]
	v_fma_mix_f32 v79, v109, v239, v79 op_sel:[1,1,0] op_sel_hi:[1,1,0]
	v_fma_mix_f32 v78, v110, v224, v78 op_sel_hi:[1,1,0]
	v_fma_mix_f32 v79, v110, v240, v79 op_sel_hi:[1,1,0]
	v_fma_mix_f32 v78, v110, v224, v78 op_sel:[1,1,0] op_sel_hi:[1,1,0]
	v_fma_mix_f32 v79, v110, v240, v79 op_sel:[1,1,0] op_sel_hi:[1,1,0]
	v_fma_mix_f32 v78, v111, v225, v78 op_sel_hi:[1,1,0]
	v_fma_mix_f32 v79, v111, v241, v79 op_sel_hi:[1,1,0]
	v_fma_mix_f32 v78, v111, v225, v78 op_sel:[1,1,0] op_sel_hi:[1,1,0]
	v_fma_mix_f32 v79, v111, v241, v79 op_sel:[1,1,0] op_sel_hi:[1,1,0]
	v_mov_b32_e32 v64, v78
	v_mov_b32_e32 v65, v79
	s_nop 1
	v_permlane32_swap_b32_e32 v78, v64
	v_permlane32_swap_b32_e32 v79, v65
	v_add_f32_e32 v78, v78, v64
	v_add_f32_e32 v79, v79, v65
	s_waitcnt lgkmcnt(0)
	v_add_f32_e32 v78, v78, v48
	v_add_f32_e32 v79, v79, v48
	v_add_f32_e32 v78, v78, v66
	v_add_f32_e32 v79, v79, v68
	s_mov_b32 s48, 0xc2200a3d
	v_cmp_ngt_f32_e32 vcc, s48, v78
	s_cmp_lg_u64 vcc, 0
	s_cselect_b32 s50, 4, 0
	v_cmp_ngt_f32_e32 vcc, s48, v79
	s_cmp_lg_u64 vcc, 0
	s_cselect_b32 s51, 0x400, 0
	s_or_b32 s50, s50, s51
	v_max3_f32 v64, v70, v71, v72
	v_max_f32_e32 v64, v64, v73
	v_fma_f32 v64, v169, v64, v67
	v_sub_f32_e32 v64, v64, v193
	v_cmp_ngt_f32_e32 vcc, s48, v64
	s_cmp_lg_u64 vcc, 0
	s_cselect_b32 s51, 4, 0
	s_or_b32 s50, s50, s51
	v_max3_f32 v65, v74, v75, v76
	v_max_f32_e32 v65, v65, v77
	v_fma_f32 v65, v169, v65, v69
	v_sub_f32_e32 v65, v65, v193
	v_cmp_ngt_f32_e32 vcc, s48, v65
	s_cmp_lg_u64 vcc, 0
	s_cselect_b32 s51, 0x400, 0
	s_or_b32 s50, s50, s51
	v_mov_b32_e32 v64, s25
	v_mov_b32_e32 v65, s50
	ds_write_b32 v64, v65 offset:32

	.amdhsa_kernel _Z8attn_fwdPKDF16_S0_S0_PKjPf
		.amdhsa_group_segment_fixed_size 132896
		.amdhsa_private_segment_fixed_size 0
		.amdhsa_kernarg_size 40
		.amdhsa_user_sgpr_count 2
		.amdhsa_user_sgpr_dispatch_ptr 0
		.amdhsa_user_sgpr_queue_ptr 0
		.amdhsa_user_sgpr_kernarg_segment_ptr 1
		.amdhsa_user_sgpr_dispatch_id 0
		.amdhsa_user_sgpr_kernarg_preload_length 0
		.amdhsa_user_sgpr_kernarg_preload_offset 0
		.amdhsa_user_sgpr_private_segment_size 0
		.amdhsa_uses_dynamic_stack 0
		.amdhsa_enable_private_segment 0
		.amdhsa_system_sgpr_workgroup_id_x 1
		.amdhsa_system_sgpr_workgroup_id_y 0
		.amdhsa_system_sgpr_workgroup_id_z 0
		.amdhsa_system_sgpr_workgroup_info 0
		.amdhsa_system_vgpr_workitem_id 0
		.amdhsa_next_free_vgpr 242
		.amdhsa_next_free_sgpr 96
		.amdhsa_accum_offset 244
		.amdhsa_reserve_vcc 1
		.amdhsa_float_round_mode_32 0
		.amdhsa_float_round_mode_16_64 0
		.amdhsa_float_denorm_mode_32 3
		.amdhsa_float_denorm_mode_16_64 3
		.amdhsa_dx10_clamp 1
		.amdhsa_ieee_mode 1
		.amdhsa_fp16_overflow 0
		.amdhsa_tg_split 0
		.amdhsa_exception_fp_ieee_invalid_op 0
		.amdhsa_exception_fp_denorm_src 0
		.amdhsa_exception_fp_ieee_div_zero 0
		.amdhsa_exception_fp_ieee_overflow 0
		.amdhsa_exception_fp_ieee_underflow 0
		.amdhsa_exception_fp_ieee_inexact 0
		.amdhsa_exception_int_div_zero 0
	.end_amdhsa_kernel

amdhsa.kernels:
  - .agpr_count:     0
    .args:
      - .actual_access:  read_only
        .address_space:  global
        .offset:         0
        .size:           8
        .value_kind:     global_buffer
      - .actual_access:  read_only
        .address_space:  global
        .offset:         8
        .size:           8
        .value_kind:     global_buffer
      - .address_space:  global
        .offset:         16
        .size:           8
        .value_kind:     global_buffer
      - .address_space:  global
        .offset:         24
        .size:           8
        .value_kind:     global_buffer
      - .offset:         32
        .size:           4
        .value_kind:     by_value
      - .actual_access:  write_only
        .address_space:  global
        .offset:         40
        .size:           8
        .value_kind:     global_buffer
    .group_segment_fixed_size: 0
    .kernarg_segment_align: 8
    .kernarg_segment_size: 48
    .language:       OpenCL C
    .language_version:
      - 2
      - 0
    .max_flat_workgroup_size: 256
    .name:           _Z7cvt_f16PKfS0_PDF16_S1_iPj
    .private_segment_fixed_size: 0
    .sgpr_count:     32
    .sgpr_spill_count: 0
    .symbol:         _Z7cvt_f16PKfS0_PDF16_S1_iPj.kd
    .uniform_work_group_size: 1
    .uses_dynamic_stack: false
    .vgpr_count:     50
    .vgpr_spill_count: 0
    .wavefront_size: 64
  - .agpr_count:     0
    .args:
      - .address_space:  global
        .offset:         0
        .size:           8
        .value_kind:     global_buffer
      - .address_space:  global
        .offset:         8
        .size:           8
        .value_kind:     global_buffer
      - .actual_access:  read_only
        .address_space:  global
        .offset:         16
        .size:           8
        .value_kind:     global_buffer
      - .address_space:  global
        .offset:         24
        .size:           8
        .value_kind:     global_buffer
      - .address_space:  global
        .offset:         32
        .size:           8
        .value_kind:     global_buffer
      - .address_space:  global
        .offset:         40
        .size:           8
        .value_kind:     global_buffer
      - .address_space:  global
        .offset:         48
        .size:           8
        .value_kind:     global_buffer
    .group_segment_fixed_size: 1024
    .kernarg_segment_align: 8
    .kernarg_segment_size: 56
    .language:       OpenCL C
    .language_version:
      - 2
      - 0
    .max_flat_workgroup_size: 512
    .name:           _Z8gemm_qkvPKDF16_S0_PKfPDF16_S3_S3_Pj
    .private_segment_fixed_size: 0
    .sgpr_count:     37
    .sgpr_spill_count: 0
    .symbol:         _Z8gemm_qkvPKDF16_S0_PKfPDF16_S3_S3_Pj.kd
    .uniform_work_group_size: 1
    .uses_dynamic_stack: false
    .vgpr_count:     256
    .vgpr_spill_count: 0
    .wavefront_size: 64
  - .agpr_count:     0
    .args:
      - .actual_access:  read_only
        .address_space:  global
        .offset:         0
        .size:           8
        .value_kind:     global_buffer
      - .address_space:  global
        .offset:         8
        .size:           8
        .value_kind:     global_buffer
      - .address_space:  global
        .offset:         16
        .size:           8
        .value_kind:     global_buffer
      - .actual_access:  read_only
        .address_space:  global
        .offset:         24
        .size:           8
        .value_kind:     global_buffer
      - .address_space:  global
        .offset:         32
        .size:           8
        .value_kind:     global_buffer
    .group_segment_fixed_size: 132896
    .kernarg_segment_align: 8
    .kernarg_segment_size: 40
    .language:       OpenCL C
    .language_version:
      - 2
      - 0
    .max_flat_workgroup_size: 512
    .name:           _Z8attn_fwdPKDF16_S0_S0_PKjPf
    .private_segment_fixed_size: 0
    .sgpr_count:     41
    .sgpr_spill_count: 0
    .symbol:         _Z8attn_fwdPKDF16_S0_S0_PKjPf.kd
    .uniform_work_group_size: 1
    .uses_dynamic_stack: false
    .vgpr_count:     242
    .vgpr_spill_count: 0
    .wavefront_size: 64
